# speedup vs baseline: 1.0604x; 1.0106x over previous
_ZN12_GLOBAL__N_110k_convpoolEPKtS1_PKfPKiPtS3_S6_:
	v_lshlrev_b32_e32 v70, 4, v0
	v_lshlrev_b32_e32 v1, 1, v0
	v_lshrrev_b32_e32 v86, 2, v0
	v_and_b32_e32 v2, 32, v1
	v_and_b32_e32 v3, 48, v70
	v_lshlrev_b32_e32 v5, 6, v86
	s_lshl_b32 s3, s2, 2
	v_bitop3_b32 v4, v1, v3, 32 bitop3:0x6c
	v_bitop3_b32 v72, v5, v2, v3 bitop3:0xf6
	v_mov_b32_e32 v3, 0x2000
	s_and_b32 s21, s3, 28
	s_ashr_i32 s3, s2, 6
	v_bitop3_b32 v3, v70, 48, v3 bitop3:0xc8
	s_add_i32 s21, s21, s3
	v_or_b32_e32 v2, 0x2000, v70
	v_bitop3_b32 v3, v1, v3, 32 bitop3:0x6c
	s_movk_i32 s3, 0x3fc0
	s_load_dwordx4 s[4:7], s[0:1], 0x0
	s_load_dwordx4 s[12:15], s[0:1], 0x28
	v_and_or_b32 v68, v2, s3, v3
	v_mov_b32_e32 v3, 0x6000
	v_and_b32_e32 v2, 0x1fc0, v70
	s_movk_i32 s3, 0x4000
	v_bitop3_b32 v3, v70, 48, v3 bitop3:0xc8
	v_readfirstlane_b32 s20, v0
	v_or3_b32 v66, v2, v4, s3
	v_or_b32_e32 v2, 0x6000, v70
	v_bitop3_b32 v1, v1, v3, 32 bitop3:0x6c
	s_movk_i32 s3, 0x7fc0
	v_and_or_b32 v74, v2, s3, v1
	v_and_b32_e32 v1, 0x3c0, v70
	s_mov_b32 s3, 0x8000
	s_bfe_u32 s22, s2, 0x30003
	s_mul_i32 s8, s21, 0x52800
	s_and_b32 s29, s20, 0x3ffffc0
	v_or3_b32 v78, v1, v4, s3
	s_mul_hi_i32 s3, s21, 0x52800
	s_waitcnt lgkmcnt(0)
	v_cmp_lt_u32_e32 vcc, 0xbf, v0
	s_mul_i32 s48, s2, 6
	s_mov_b32 s49, 0x18000
	v_cndmask_b32_e64 v200, 0, 1, vcc
	v_mul_u32_u24_e32 v201, 0xc0, v200
	v_sub_u32_e32 v201, v0, v201
	v_add_u32_e32 v200, s48, v200
	v_lshlrev_b32_e32 v200, 6, v200
	v_and_b32_e32 v202, 3, v201
	v_lshl_add_u32 v200, v202, 4, v200
	v_lshrrev_b32_e32 v201, 2, v201
	v_mul_lo_u32 v201, v201, s49
	v_add_u32_e32 v200, v200, v201
	v_mov_b32_e32 v201, 0
	v_lshl_add_u64 v[200:201], s[14:15], 0, v[200:201]
	s_add_u32 s10, s4, s8
	s_addc_u32 s11, s5, s3
	s_lshl_b32 s30, s20, 4
	s_mul_i32 s9, s22, 0x1e000
	s_and_b32 s3, s30, 0xfffffc00
	s_add_u32 s16, s6, s9
	s_addc_u32 s17, s7, 0
	s_add_i32 s28, s3, 0
	s_add_i32 s27, s28, 0x2000
	s_add_i32 s26, s28, 0x4000
	s_add_i32 s23, s28, 0x6000
	s_cmp_lt_u32 s20, 64
	s_cselect_b64 s[6:7], -1, 0
	s_add_i32 s24, s28, 0x8000
	s_cmpk_lt_u32 s20, 0x140
	s_cselect_b64 s[8:9], -1, 0
	s_mov_b32 m0, s28
	s_and_b64 s[4:5], s[8:9], exec
	v_mov_b32_e32 v73, 0
	global_load_lds_dwordx4 v72, s[10:11]
	s_mov_b32 m0, s27
	s_cselect_b32 s3, 0xa000, 0
	v_add_u32_e32 v80, 0xfffffc00, v70
	global_load_lds_dwordx4 v68, s[10:11]
	s_mov_b32 m0, s26
	v_mov_b32_e32 v79, v73
	v_mov_b32_e32 v81, v73
	s_add_i32 s25, s28, s3
	global_load_lds_dwordx4 v66, s[10:11]
	s_mov_b32 m0, s23
	v_lshl_add_u64 v[4:5], s[10:11], 0, v[78:79]
	v_lshl_add_u64 v[6:7], s[16:17], 0, v[80:81]
	s_add_u32 s4, s10, 0x8400
	v_add_u32_e32 v76, 0x1c00, v70
	global_load_lds_dwordx4 v74, s[10:11]
	v_cndmask_b32_e64 v5, v7, v5, s[6:7]
	v_cndmask_b32_e64 v4, v6, v4, s[6:7]
	s_mov_b32 m0, s24
	v_mov_b32_e32 v77, v73
	s_addc_u32 s5, s11, 0
	v_lshl_add_u64 v[2:3], s[10:11], 0, v[72:73]
	global_load_lds_dwordx4 v[4:5], off
	v_lshl_add_u64 v[4:5], s[16:17], 0, v[76:77]
	s_add_u32 s18, s16, 0x3000
	v_cndmask_b32_e64 v3, v3, v5, s[8:9]
	v_cndmask_b32_e64 v2, v2, v4, s[8:9]
	s_mov_b32 m0, s25
	s_addc_u32 s19, s17, 0
	s_add_i32 s43, s28, 0xb400
	global_load_lds_dwordx4 v[2:3], off
	s_mov_b32 m0, s43
	s_add_i32 s42, s28, 0xd400
	global_load_lds_dwordx4 v72, s[4:5]
	s_mov_b32 m0, s42
	s_add_i32 s39, s28, 0xf400
	global_load_lds_dwordx4 v68, s[4:5]
	s_mov_b32 m0, s39
	s_add_i32 s36, s28, 0x11400
	global_load_lds_dwordx4 v66, s[4:5]
	s_mov_b32 m0, s36
	v_lshl_add_u64 v[2:3], s[4:5], 0, v[72:73]
	global_load_lds_dwordx4 v74, s[4:5]
	v_lshl_add_u64 v[4:5], s[4:5], 0, v[78:79]
	s_mul_hi_i32 s5, s2, 0x2400
	s_mul_i32 s4, s2, 0x2400
	s_add_i32 s37, s28, 0x13400
	s_add_i32 s35, s25, 0xb400
	s_lshl_b64 s[2:3], s[4:5], 2
	s_add_u32 s2, s12, s2
	v_lshl_add_u64 v[6:7], s[18:19], 0, v[80:81]
	s_addc_u32 s3, s13, s3
	s_lshl_b64 s[4:5], s[4:5], 1
	v_cndmask_b32_e64 v5, v7, v5, s[6:7]
	v_cndmask_b32_e64 v4, v6, v4, s[6:7]
	s_mov_b32 m0, s37
	s_add_u32 s12, s14, s4
	v_lshlrev_b32_e32 v123, 2, v0
	global_load_lds_dwordx4 v[4:5], off
	v_lshl_add_u64 v[4:5], s[18:19], 0, v[76:77]
	s_addc_u32 s13, s15, s5
	v_and_b32_e32 v1, 0x3fc, v123
	s_and_b32 s4, s30, 0xc00
	v_cndmask_b32_e64 v3, v3, v5, s[8:9]
	v_cndmask_b32_e64 v2, v2, v4, s[8:9]
	s_mov_b32 m0, s35
	s_add_i32 s38, s28, 0x22910
	s_add_i32 s33, s4, 0
	v_lshlrev_b32_e32 v84, 2, v1
	v_mov_b32_e32 v85, v73
	global_load_lds_dwordx4 v[2:3], off
	s_add_i32 s33, s33, 0x24910
	s_mov_b32 m0, s38
	v_lshl_add_u64 v[2:3], s[2:3], 0, v[84:85]
	s_mov_b64 s[18:19], 0x2000
	s_waitcnt vmcnt(6)
	s_barrier
	s_cmp_lt_u32 s20, 0x100
	s_cbranch_scc1 .Lcp_noprio
	s_setprio 1
.Lcp_noprio:
	global_load_lds_dwordx4 v70, s[2:3] nt
	v_lshl_add_u64 v[2:3], v[2:3], 0, s[18:19]
	s_mov_b32 m0, s33
	v_and_b32_e32 v89, 15, v0
	global_load_lds_dwordx4 v[2:3], off nt
	v_or_b32_e32 v2, s29, v89
	v_add_u32_e32 v6, 1, v2
	v_lshlrev_b32_e32 v7, 6, v6
	v_lshlrev_b32_e32 v6, 3, v6
	v_and_b32_e32 v88, 48, v0
	v_and_b32_e32 v8, 0x3c0, v7
	v_and_b32_e32 v6, 32, v6
	v_lshlrev_b32_e32 v1, 6, v2
	v_bitop3_b32 v6, v8, v6, v88 bitop3:0x36
	s_movk_i32 s4, 0xf400
	v_add_u32_e32 v2, 2, v2
	v_and_or_b32 v94, v7, s4, v6
	v_lshlrev_b32_e32 v6, 6, v2
	v_lshlrev_b32_e32 v2, 3, v2
	v_and_b32_e32 v3, 0x3c0, v1
	v_and_b32_e32 v4, 0xfffff000, v1
	v_lshlrev_b32_e32 v1, 3, v0
	v_and_b32_e32 v7, 0x3c0, v6
	v_and_b32_e32 v2, 32, v2
	v_and_b32_e32 v5, 32, v1
	v_bitop3_b32 v2, v7, v2, v88 bitop3:0x36
	v_bitop3_b32 v3, v3, v5, v88 bitop3:0x36
	v_and_or_b32 v102, v6, s4, v2
	v_lshl_or_b32 v2, v89, 6, v88
	v_add3_u32 v91, 0, v3, v4
	v_xad_u32 v90, v2, v5, 0
	v_mov_b32_e32 v71, v73
	v_lshl_add_u64 v[82:83], s[12:13], 0, v[70:71]
	ds_read_b128 v[2:5], v91
	ds_read_b128 v[6:9], v91 offset:1024
	ds_read_b128 v[10:13], v91 offset:2048
	ds_read_b128 v[14:17], v91 offset:3072
	s_add_u32 s12, s16, 0x6000
	ds_read_b128 v[18:21], v90 offset:33792
	ds_read_b128 v[22:25], v90 offset:34816
	ds_read_b128 v[26:29], v90 offset:35840
	ds_read_b128 v[30:33], v90 offset:36864
	s_addc_u32 s13, s17, 0
	v_add_u32_e32 v71, 0, v94
	s_add_u32 s14, s10, 0x10800
	ds_read_b128 v[42:45], v71
	ds_read_b128 v[46:49], v71 offset:1024
	ds_read_b128 v[50:53], v71 offset:2048
	ds_read_b128 v[54:57], v71 offset:3072
	ds_read_b128 v[62:65], v90 offset:37888
	ds_read_b128 v[96:99], v90 offset:38912
	ds_read_b128 v[104:107], v90 offset:39936
	ds_read_b128 v[108:111], v90 offset:40960
	s_addc_u32 s15, s11, 0
	v_lshl_add_u64 v[34:35], s[14:15], 0, v[78:79]
	v_lshl_add_u64 v[36:37], s[12:13], 0, v[80:81]
	v_lshl_add_u64 v[38:39], s[12:13], 0, v[76:77]
	v_lshl_add_u64 v[40:41], s[14:15], 0, v[72:73]
	v_cndmask_b32_e64 v101, v37, v35, s[6:7]
	v_cndmask_b32_e64 v100, v36, v34, s[6:7]
	s_waitcnt lgkmcnt(0)
	v_mfma_f32_16x16x32_f16 v[34:37], v[18:21], v[2:5], 0
	v_cndmask_b32_e64 v121, v41, v39, s[8:9]
	v_cndmask_b32_e64 v120, v40, v38, s[8:9]
	s_movk_i32 s4, 0x180
	v_mfma_f32_16x16x32_f16 v[38:41], v[22:25], v[2:5], 0
	v_mov_b32_e32 v69, v73
	v_mov_b32_e32 v67, v73
	v_mov_b32_e32 v75, v73
	v_mfma_f32_16x16x32_f16 v[58:61], v[26:29], v[2:5], 0
	v_cmp_gt_u32_e64 s[4:5], s4, v0
	s_add_i32 s34, s28, 0x16800
	s_add_i32 s30, s28, 0x1e800
	v_mfma_f32_16x16x32_f16 v[2:5], v[30:33], v[2:5], 0
	s_add_i32 s31, s28, 0x1c800
	s_add_i32 s29, s25, 0x16800
	v_lshlrev_b32_e32 v87, 5, v0
	s_mov_b32 m0, s34
	s_nop 0
	global_load_lds_dwordx4 v72, s[14:15]
	v_mfma_f32_16x16x32_f16 v[112:115], v[18:21], v[6:9], 0
	s_add_i32 s40, s28, 0x18800
	v_mfma_f32_16x16x32_f16 v[116:119], v[22:25], v[6:9], 0
	v_mfma_f32_16x16x32_f16 v[124:127], v[26:29], v[6:9], 0
	v_mfma_f32_16x16x32_f16 v[6:9], v[30:33], v[6:9], 0
	s_mov_b32 m0, s40
	s_nop 0
	global_load_lds_dwordx4 v68, s[14:15]
	v_mfma_f32_16x16x32_f16 v[128:131], v[18:21], v[10:13], 0
	s_add_i32 s41, s28, 0x1a800
	v_mfma_f32_16x16x32_f16 v[132:135], v[22:25], v[10:13], 0
	v_mfma_f32_16x16x32_f16 v[136:139], v[26:29], v[10:13], 0
	v_mfma_f32_16x16x32_f16 v[10:13], v[30:33], v[10:13], 0
	s_mov_b32 m0, s41
	s_nop 0
	global_load_lds_dwordx4 v66, s[14:15]
	v_add_u32_e32 v92, 0, v102
	v_mfma_f32_16x16x32_f16 v[18:21], v[18:21], v[14:17], 0
	v_mfma_f32_16x16x32_f16 v[22:25], v[22:25], v[14:17], 0
	v_mfma_f32_16x16x32_f16 v[26:29], v[26:29], v[14:17], 0
	v_mfma_f32_16x16x32_f16 v[14:17], v[30:33], v[14:17], 0
	v_mfma_f32_16x16x32_f16 v[30:33], v[62:65], v[42:45], v[34:37]
	v_mfma_f32_16x16x32_f16 v[34:37], v[96:99], v[42:45], v[38:41]
	s_nop 2
	ds_read_b128 v[38:41], v92
	ds_read_b128 v[140:143], v92 offset:1024
	ds_read_b128 v[144:147], v92 offset:2048
	ds_read_b128 v[148:151], v92 offset:3072
	ds_read_b128 v[152:155], v90 offset:41984
	ds_read_b128 v[156:159], v90 offset:43008
	ds_read_b128 v[160:163], v90 offset:44032
	ds_read_b128 v[164:167], v90 offset:45056
	v_mfma_f32_16x16x32_f16 v[58:61], v[104:107], v[42:45], v[58:61]
	v_mfma_f32_16x16x32_f16 v[2:5], v[108:111], v[42:45], v[2:5]
	s_mov_b32 m0, s31
	s_nop 0
	global_load_lds_dwordx4 v74, s[14:15]
	v_mfma_f32_16x16x32_f16 v[42:45], v[62:65], v[46:49], v[112:115]
	v_mfma_f32_16x16x32_f16 v[112:115], v[96:99], v[46:49], v[116:119]
	v_mfma_f32_16x16x32_f16 v[116:119], v[104:107], v[46:49], v[124:127]
	v_mfma_f32_16x16x32_f16 v[6:9], v[108:111], v[46:49], v[6:9]
	s_mov_b32 m0, s30
	s_nop 0
	global_load_lds_dwordx4 v[100:101], off
	v_mfma_f32_16x16x32_f16 v[46:49], v[62:65], v[50:53], v[128:131]
	v_mfma_f32_16x16x32_f16 v[124:127], v[96:99], v[50:53], v[132:135]
	v_mfma_f32_16x16x32_f16 v[128:131], v[104:107], v[50:53], v[136:139]
	v_mfma_f32_16x16x32_f16 v[10:13], v[108:111], v[50:53], v[10:13]
	v_mfma_f32_16x16x32_f16 v[18:21], v[62:65], v[54:57], v[18:21]
	v_mfma_f32_16x16x32_f16 v[22:25], v[96:99], v[54:57], v[22:25]
	v_mfma_f32_16x16x32_f16 v[26:29], v[104:107], v[54:57], v[26:29]
	v_mfma_f32_16x16x32_f16 v[14:17], v[108:111], v[54:57], v[14:17]
	s_waitcnt lgkmcnt(0)
	v_mfma_f32_16x16x32_f16 v[30:33], v[152:155], v[38:41], v[30:33]
	v_mfma_f32_16x16x32_f16 v[34:37], v[156:159], v[38:41], v[34:37]
	v_mfma_f32_16x16x32_f16 v[50:53], v[160:163], v[38:41], v[58:61]
	v_mfma_f32_16x16x32_f16 v[2:5], v[164:167], v[38:41], v[2:5]
	s_mov_b32 m0, s29
	s_nop 0
	global_load_lds_dwordx4 v[120:121], off
	s_add_u32 s12, s16, 0x9000
	s_addc_u32 s13, s17, 0
	s_waitcnt vmcnt(8)
	v_add_u32_e32 v99, 0x13800, v90
	v_add_u32_e32 v101, 0x14000, v90
	s_add_u32 s14, s10, 0x18c00
	v_mfma_f32_16x16x32_f16 v[38:41], v[152:155], v[140:143], v[42:45]
	s_waitcnt lgkmcnt(0)
	s_barrier
	ds_read_b128 v[58:61], v91 offset:46080
	ds_read_b128 v[62:65], v91 offset:47104
	v_mfma_f32_16x16x32_f16 v[42:45], v[156:159], v[140:143], v[112:115]
	v_add_u32_e32 v100, 0x13c00, v90
	v_add_u32_e32 v103, 0x14400, v90
	s_addc_u32 s15, s11, 0
	v_mfma_f32_16x16x32_f16 v[54:57], v[160:163], v[140:143], v[116:119]
	ds_read_b128 v[106:109], v91 offset:48128
	s_nop 1
	ds_read_b128 v[116:119], v91 offset:49152
	ds_read_b128 v[132:135], v99
	ds_read_b128 v[136:139], v100
	v_lshl_add_u64 v[96:97], s[14:15], 0, v[78:79]
	v_mfma_f32_16x16x32_f16 v[6:9], v[164:167], v[140:143], v[6:9]
	v_lshl_add_u64 v[104:105], s[12:13], 0, v[80:81]
	v_cndmask_b32_e64 v97, v105, v97, s[6:7]
	v_cndmask_b32_e64 v96, v104, v96, s[6:7]
	v_mfma_f32_16x16x32_f16 v[46:49], v[152:155], v[144:147], v[46:49]
	v_lshl_add_u64 v[104:105], s[12:13], 0, v[76:77]
	v_lshl_add_u64 v[110:111], s[14:15], 0, v[72:73]
	v_cndmask_b32_e64 v113, v111, v105, s[8:9]
	v_mfma_f32_16x16x32_f16 v[124:127], v[156:159], v[144:147], v[124:127]
	v_cndmask_b32_e64 v112, v110, v104, s[8:9]
	v_add_u32_e32 v104, 0x14800, v90
	v_add_u32_e32 v111, 0x15000, v90
	v_mfma_f32_16x16x32_f16 v[128:131], v[160:163], v[144:147], v[128:131]
	v_add_u32_e32 v105, 0x14c00, v90
	v_add_u32_e32 v114, 0x15400, v90
	v_mfma_f32_16x16x32_f16 v[10:13], v[164:167], v[144:147], v[10:13]
	ds_read_b128 v[140:143], v101
	ds_read_b128 v[144:147], v103
	v_mfma_f32_16x16x32_f16 v[18:21], v[152:155], v[148:151], v[18:21]
	v_mfma_f32_16x16x32_f16 v[22:25], v[156:159], v[148:151], v[22:25]
	v_mfma_f32_16x16x32_f16 v[26:29], v[160:163], v[148:151], v[26:29]
	v_mfma_f32_16x16x32_f16 v[14:17], v[164:167], v[148:151], v[14:17]
	ds_read_b128 v[148:151], v71 offset:46080
	ds_read_b128 v[152:155], v71 offset:47104
	ds_read_b128 v[156:159], v71 offset:48128
	ds_read_b128 v[160:163], v71 offset:49152
	ds_read_b128 v[164:167], v104
	ds_read_b128 v[168:171], v105
	ds_read_b128 v[172:175], v111
	ds_read_b128 v[176:179], v114
	s_waitcnt lgkmcnt(0)
	v_mfma_f32_16x16x32_f16 v[30:33], v[132:135], v[58:61], v[30:33]
	v_mfma_f32_16x16x32_f16 v[34:37], v[136:139], v[58:61], v[34:37]
	v_mfma_f32_16x16x32_f16 v[50:53], v[140:143], v[58:61], v[50:53]
	v_mfma_f32_16x16x32_f16 v[2:5], v[144:147], v[58:61], v[2:5]
	s_mov_b32 m0, s28
	s_nop 0
	global_load_lds_dwordx4 v72, s[14:15]
	v_mfma_f32_16x16x32_f16 v[38:41], v[132:135], v[62:65], v[38:41]
	v_mfma_f32_16x16x32_f16 v[42:45], v[136:139], v[62:65], v[42:45]
	v_mfma_f32_16x16x32_f16 v[54:57], v[140:143], v[62:65], v[54:57]
	v_mfma_f32_16x16x32_f16 v[6:9], v[144:147], v[62:65], v[6:9]
	s_mov_b32 m0, s27
	s_nop 0
	global_load_lds_dwordx4 v68, s[14:15]
	v_mfma_f32_16x16x32_f16 v[46:49], v[132:135], v[106:109], v[46:49]
	v_mfma_f32_16x16x32_f16 v[58:61], v[136:139], v[106:109], v[124:127]
	v_mfma_f32_16x16x32_f16 v[62:65], v[140:143], v[106:109], v[128:131]
	v_mfma_f32_16x16x32_f16 v[10:13], v[144:147], v[106:109], v[10:13]
	s_mov_b32 m0, s26
	s_nop 0
	global_load_lds_dwordx4 v66, s[14:15]
	v_add_u32_e32 v108, 0x15800, v90
	v_add_u32_e32 v115, 0x16000, v90
	v_mfma_f32_16x16x32_f16 v[18:21], v[132:135], v[116:119], v[18:21]
	v_add_u32_e32 v109, 0x15c00, v90
	v_mfma_f32_16x16x32_f16 v[22:25], v[136:139], v[116:119], v[22:25]
	v_mfma_f32_16x16x32_f16 v[26:29], v[140:143], v[116:119], v[26:29]
	v_mfma_f32_16x16x32_f16 v[14:17], v[144:147], v[116:119], v[14:17]
	ds_read_b128 v[118:121], v92 offset:46080
	ds_read_b128 v[124:127], v92 offset:47104
	ds_read_b128 v[128:131], v92 offset:48128
	ds_read_b128 v[132:135], v92 offset:49152
	ds_read_b128 v[136:139], v108
	ds_read_b128 v[140:143], v109
	v_add_u32_e32 v116, 0x16400, v90
	ds_read_b128 v[144:147], v115
	ds_read_b128 v[180:183], v116
	v_mfma_f32_16x16x32_f16 v[30:33], v[164:167], v[148:151], v[30:33]
	v_mfma_f32_16x16x32_f16 v[34:37], v[168:171], v[148:151], v[34:37]
	v_mfma_f32_16x16x32_f16 v[50:53], v[172:175], v[148:151], v[50:53]
	v_mfma_f32_16x16x32_f16 v[2:5], v[176:179], v[148:151], v[2:5]
	s_mov_b32 m0, s23
	s_nop 0
	global_load_lds_dwordx4 v74, s[14:15]
	v_mfma_f32_16x16x32_f16 v[6:9], v[176:179], v[152:155], v[6:9]
	v_mfma_f32_16x16x32_f16 v[148:151], v[164:167], v[152:155], v[38:41]
	v_mfma_f32_16x16x32_f16 v[184:187], v[168:171], v[152:155], v[42:45]
	v_mfma_f32_16x16x32_f16 v[188:191], v[172:175], v[152:155], v[54:57]
	s_mov_b32 m0, s24
	s_nop 0
	global_load_lds_dwordx4 v[96:97], off
	v_mfma_f32_16x16x32_f16 v[192:195], v[168:171], v[156:159], v[58:61]
	v_mfma_f32_16x16x32_f16 v[196:199], v[172:175], v[156:159], v[62:65]
	v_mfma_f32_16x16x32_f16 v[10:13], v[176:179], v[156:159], v[10:13]
	v_mfma_f32_16x16x32_f16 v[18:21], v[164:167], v[160:163], v[18:21]
	s_waitcnt lgkmcnt(0)
	v_mfma_f32_16x16x32_f16 v[62:65], v[136:139], v[118:121], v[30:33]
	v_mfma_f32_16x16x32_f16 v[58:61], v[140:143], v[118:121], v[34:37]
	v_mfma_f32_16x16x32_f16 v[54:57], v[144:147], v[118:121], v[50:53]
	v_mfma_f32_16x16x32_f16 v[38:41], v[180:183], v[118:121], v[2:5]
	v_mfma_f32_16x16x32_f16 v[152:155], v[164:167], v[156:159], v[46:49]
	v_mfma_f32_16x16x32_f16 v[156:159], v[168:171], v[160:163], v[22:25]
	v_mfma_f32_16x16x32_f16 v[164:167], v[172:175], v[160:163], v[26:29]
	v_mfma_f32_16x16x32_f16 v[160:163], v[176:179], v[160:163], v[14:17]
	s_mov_b32 m0, s25
	s_nop 0
	global_load_lds_dwordx4 v[112:113], off
	v_mfma_f32_16x16x32_f16 v[42:45], v[136:139], v[124:127], v[148:151]
	s_waitcnt vmcnt(6)
	s_waitcnt lgkmcnt(0)
	v_add_u32_e32 v107, 0, v87
	v_mfma_f32_16x16x32_f16 v[46:49], v[140:143], v[124:127], v[184:187]
	s_barrier
	v_mfma_f32_16x16x32_f16 v[50:53], v[144:147], v[124:127], v[188:191]
	v_mfma_f32_16x16x32_f16 v[34:37], v[180:183], v[124:127], v[6:9]
	v_mfma_f32_16x16x32_f16 v[22:25], v[136:139], v[128:131], v[152:155]
	v_mfma_f32_16x16x32_f16 v[26:29], v[140:143], v[128:131], v[192:195]
	v_mfma_f32_16x16x32_f16 v[30:33], v[144:147], v[128:131], v[196:199]
	v_mfma_f32_16x16x32_f16 v[14:17], v[180:183], v[128:131], v[10:13]
	v_mfma_f32_16x16x32_f16 v[2:5], v[136:139], v[132:135], v[18:21]
	v_mfma_f32_16x16x32_f16 v[6:9], v[140:143], v[132:135], v[156:159]
	v_mfma_f32_16x16x32_f16 v[10:13], v[144:147], v[132:135], v[164:167]
	v_mfma_f32_16x16x32_f16 v[18:21], v[180:183], v[132:135], v[160:163]
	s_and_saveexec_b64 s[12:13], s[4:5]
	s_cbranch_execz .LBB2_2
	v_add_u32_e32 v87, 0x22910, v107
	ds_read_b128 v[118:121], v87 offset:16
	ds_read_b128 v[124:127], v87
	s_waitcnt lgkmcnt(0)
	v_cvt_pk_f16_f32 v121, v120, v121
	v_cvt_pk_f16_f32 v120, v118, v119
	v_cvt_pk_f16_f32 v119, v126, v127
	v_cvt_pk_f16_f32 v118, v124, v125
	global_store_dwordx4 v[200:201], v[118:121], off

.LBB2_6:
	s_or_b64 exec, exec, s[2:3]
	ds_read_b128 v[66:69], v106
	ds_read_b128 v[72:75], v110
	ds_read_b128 v[76:79], v95
	ds_read_b128 v[80:83], v96
	ds_read_b128 v[104:107], v97
	ds_read_b128 v[96:99], v98
	s_lshl_b32 s5, s21, 9
	s_waitcnt lgkmcnt(0)
	v_mfma_f32_16x16x32_f16 v[14:17], v[66:69], v[76:79], v[14:17]
	s_and_b32 s2, s20, 0x7fffffc0
	s_add_i32 s2, s2, s5
	s_lshl_b32 s9, s22, 6
	v_mfma_f32_16x16x32_f16 v[10:13], v[72:75], v[76:79], v[10:13]
	v_mfma_f32_16x16x32_f16 v[2:5], v[104:107], v[76:79], v[2:5]
	v_mfma_f32_16x16x32_f16 v[6:9], v[96:99], v[76:79], v[6:9]
	v_mfma_f32_16x16x32_f16 v[46:49], v[66:69], v[80:83], v[46:49]
	v_mfma_f32_16x16x32_f16 v[50:53], v[72:75], v[80:83], v[50:53]
	v_mfma_f32_16x16x32_f16 v[54:57], v[104:107], v[80:83], v[54:57]
	v_mfma_f32_16x16x32_f16 v[58:61], v[96:99], v[80:83], v[58:61]
	ds_read_b128 v[76:79], v87
	ds_read_b128 v[80:83], v93
	v_bfe_u32 v93, v0, 3, 3
	s_waitcnt lgkmcnt(0)
	v_mfma_f32_16x16x32_f16 v[18:21], v[66:69], v[76:79], v[18:21]
	v_mfma_f32_16x16x32_f16 v[22:25], v[72:75], v[76:79], v[22:25]
	v_mfma_f32_16x16x32_f16 v[26:29], v[104:107], v[76:79], v[26:29]
	v_mfma_f32_16x16x32_f16 v[30:33], v[96:99], v[76:79], v[30:33]
	v_mfma_f32_16x16x32_f16 v[34:37], v[66:69], v[80:83], v[34:37]
	v_mfma_f32_16x16x32_f16 v[38:41], v[72:75], v[80:83], v[38:41]
	ds_read_b128 v[66:69], v117
	ds_read_b128 v[72:75], v118
	v_mfma_f32_16x16x32_f16 v[42:45], v[104:107], v[80:83], v[42:45]
	v_mfma_f32_16x16x32_f16 v[62:65], v[96:99], v[80:83], v[62:65]
	ds_read_b128 v[76:79], v94
	ds_read_b128 v[80:83], v94 offset:1024
	ds_read_b128 v[96:99], v112
	ds_read_b128 v[104:107], v113
	s_waitcnt lgkmcnt(0)
	v_mfma_f32_16x16x32_f16 v[14:17], v[66:69], v[76:79], v[14:17]
	v_mfma_f32_16x16x32_f16 v[10:13], v[72:75], v[76:79], v[10:13]
	v_mfma_f32_16x16x32_f16 v[2:5], v[96:99], v[76:79], v[2:5]
	v_mfma_f32_16x16x32_f16 v[6:9], v[104:107], v[76:79], v[6:9]
	v_mfma_f32_16x16x32_f16 v[46:49], v[66:69], v[80:83], v[46:49]
	v_mfma_f32_16x16x32_f16 v[50:53], v[72:75], v[80:83], v[50:53]
	v_mfma_f32_16x16x32_f16 v[54:57], v[96:99], v[80:83], v[54:57]
	v_mfma_f32_16x16x32_f16 v[58:61], v[104:107], v[80:83], v[58:61]
	ds_read_b128 v[76:79], v94 offset:2048
	ds_read_b128 v[80:83], v94 offset:3072
	s_waitcnt lgkmcnt(0)
	v_mfma_f32_16x16x32_f16 v[18:21], v[66:69], v[76:79], v[18:21]
	v_mfma_f32_16x16x32_f16 v[22:25], v[72:75], v[76:79], v[22:25]
	v_mfma_f32_16x16x32_f16 v[26:29], v[96:99], v[76:79], v[26:29]
	v_mfma_f32_16x16x32_f16 v[30:33], v[104:107], v[76:79], v[30:33]
	v_mfma_f32_16x16x32_f16 v[34:37], v[66:69], v[80:83], v[34:37]
	v_mfma_f32_16x16x32_f16 v[38:41], v[72:75], v[80:83], v[38:41]
	ds_read_b128 v[66:69], v121
	ds_read_b128 v[72:75], v122
	v_mfma_f32_16x16x32_f16 v[42:45], v[96:99], v[80:83], v[42:45]
	v_mfma_f32_16x16x32_f16 v[62:65], v[104:107], v[80:83], v[62:65]
	ds_read_b128 v[76:79], v102
	ds_read_b128 v[80:83], v102 offset:1024
	ds_read_b128 v[94:97], v119
	ds_read_b128 v[104:107], v120
	s_waitcnt lgkmcnt(0)
	v_mfma_f32_16x16x32_f16 v[108:111], v[94:97], v[76:79], v[2:5]
	s_nop 2
	ds_read_b128 v[2:5], v102 offset:2048
	v_mfma_f32_16x16x32_f16 v[112:115], v[104:107], v[76:79], v[6:9]
	s_nop 2
	ds_read_b128 v[6:9], v102 offset:3072
	v_mfma_f32_16x16x32_f16 v[98:101], v[72:75], v[76:79], v[10:13]
	s_waitcnt vmcnt(0)
	s_waitcnt lgkmcnt(0)
	s_barrier
	v_mfma_f32_16x16x32_f16 v[116:119], v[94:97], v[80:83], v[54:57]
	s_nop 0
	v_and_b32_e32 v10, 12, v86
	s_nop 0
	v_or_b32_e32 v54, s2, v93
	s_waitcnt lgkmcnt(0)
	v_mfma_f32_16x16x32_f16 v[124:127], v[66:69], v[2:5], v[18:21]
	s_lshl_b32 s2, s22, 8
	s_add_u32 s2, s12, s2
	s_addc_u32 s3, s13, 0
	v_mfma_f32_16x16x32_f16 v[128:131], v[72:75], v[2:5], v[22:25]
	v_lshlrev_b32_e32 v18, 2, v10
	v_mfma_f32_16x16x32_f16 v[132:135], v[94:97], v[2:5], v[26:29]
	v_mfma_f32_16x16x32_f16 v[10:13], v[104:107], v[2:5], v[30:33]
	v_lshlrev_b32_e32 v2, 1, v54
	v_ashrrev_i32_e32 v3, 31, v2
	v_lshl_add_u64 v[2:3], v[2:3], 2, s[14:15]
	v_mfma_f32_16x16x32_f16 v[14:17], v[66:69], v[76:79], v[14:17]
	v_mfma_f32_16x16x32_f16 v[46:49], v[66:69], v[80:83], v[46:49]
	v_mfma_f32_16x16x32_f16 v[50:53], v[72:75], v[80:83], v[50:53]
	v_mfma_f32_16x16x32_f16 v[120:123], v[104:107], v[80:83], v[58:61]
	global_load_dwordx2 v[86:87], v[2:3], off
	global_load_dwordx2 v[84:85], v[2:3], off offset:64
	global_load_dwordx2 v[82:83], v[2:3], off offset:128
	global_load_dwordx2 v[80:81], v[2:3], off offset:192
	v_mfma_f32_16x16x32_f16 v[136:139], v[66:69], v[6:9], v[34:37]
	v_mfma_f32_16x16x32_f16 v[140:143], v[72:75], v[6:9], v[38:41]
	global_load_dwordx2 v[78:79], v[2:3], off offset:256
	global_load_dwordx2 v[76:77], v[2:3], off offset:320
	global_load_dwordx2 v[74:75], v[2:3], off offset:384
	global_load_dwordx2 v[72:73], v[2:3], off offset:448
	global_load_dwordx4 v[148:151], v18, s[2:3]
	global_load_dwordx4 v[152:155], v18, s[2:3] offset:64
	global_load_dwordx4 v[34:37], v18, s[2:3] offset:128
	s_nop 0
	global_load_dwordx4 v[2:5], v18, s[2:3] offset:192
	v_mfma_f32_16x16x32_f16 v[144:147], v[94:97], v[6:9], v[42:45]
	v_and_b32_e32 v94, 63, v0
	v_mfma_f32_16x16x32_f16 v[6:9], v[104:107], v[6:9], v[62:65]
	ds_read_b128 v[102:105], v90 offset:33792
	ds_read_b128 v[156:159], v90 offset:34816
	ds_read_b128 v[18:21], v91
	ds_read_b128 v[30:33], v91 offset:1024
	ds_read_b128 v[164:167], v90 offset:35840
	s_and_b32 s8, s20, 0xffffffc0
	s_movk_i32 s4, 0x110
	s_waitcnt lgkmcnt(0)
	v_mfma_f32_16x16x32_f16 v[160:163], v[102:105], v[18:21], v[14:17]
	v_cmp_gt_u32_e32 vcc, 16, v0
	s_nop 1
	ds_read_b128 v[14:17], v90 offset:36864
	v_mfma_f32_16x16x32_f16 v[96:99], v[156:159], v[18:21], v[98:101]
	v_mfma_f32_16x16x32_f16 v[106:109], v[164:167], v[18:21], v[108:111]
	s_waitcnt lgkmcnt(0)
	v_mfma_f32_16x16x32_f16 v[54:57], v[14:17], v[18:21], v[112:115]
	v_mfma_f32_16x16x32_f16 v[110:113], v[102:105], v[30:33], v[46:49]
	ds_read_b128 v[66:69], v91 offset:2048
	ds_read_b128 v[18:21], v91 offset:3072
	ds_read_b128 v[58:61], v71
	ds_read_b128 v[46:49], v71 offset:1024
	ds_read_b128 v[42:45], v71 offset:2048
	ds_read_b128 v[22:25], v71 offset:3072
	ds_read_b128 v[172:175], v90 offset:37888
	ds_read_b128 v[176:179], v90 offset:38912
	ds_read_b128 v[180:183], v90 offset:39936
	ds_read_b128 v[26:29], v90 offset:40960
	ds_read_b128 v[184:187], v92
	ds_read_b128 v[62:65], v92 offset:1024
	v_mfma_f32_16x16x32_f16 v[168:171], v[156:159], v[30:33], v[50:53]
	v_or_b32_e32 v71, s8, v89
	v_mul_lo_u32 v71, v71, s4
	v_add3_u32 v71, 0, v71, v88
	v_mfma_f32_16x16x32_f16 v[114:117], v[164:167], v[30:33], v[116:119]
	v_mfma_f32_16x16x32_f16 v[118:121], v[14:17], v[30:33], v[120:123]
	ds_read_b128 v[50:53], v92 offset:2048
	ds_read_b128 v[30:33], v92 offset:3072
	ds_read_b128 v[188:191], v90 offset:41984
	ds_read_b128 v[192:195], v90 offset:43008
	ds_read_b128 v[196:199], v90 offset:44032
	ds_read_b128 v[38:41], v90 offset:45056
	s_waitcnt vmcnt(0)
	s_waitcnt lgkmcnt(0)
	v_mfma_f32_16x16x32_f16 v[160:163], v[172:175], v[58:61], v[160:163]
	s_waitcnt lgkmcnt(0)
	s_barrier
	s_waitcnt vmcnt(0)
	v_mfma_f32_16x16x32_f16 v[160:163], v[188:191], v[184:187], v[160:163]
	s_barrier
	s_setprio 0
	v_mfma_f32_16x16x32_f16 v[110:113], v[172:175], v[46:49], v[110:113]
	v_mfma_f32_16x16x32_f16 v[122:125], v[102:105], v[66:69], v[124:127]
	s_nop 4
	v_add_f32_e64 v90, v162, v150
	v_add_f32_e64 v91, v163, v151
	v_pk_add_f32 v[100:101], v[160:161], v[148:149]
	v_mfma_f32_16x16x32_f16 v[160:163], v[164:167], v[66:69], v[132:135]
	s_nop 2
	v_max_f32_e32 v132, 0, v90
	v_max_f32_e32 v133, 0, v91
	v_mfma_f32_16x16x32_f16 v[88:91], v[188:191], v[62:65], v[110:113]
	v_mfma_f32_16x16x32_f16 v[126:129], v[156:159], v[66:69], v[128:131]
	s_nop 2
	v_max_f32_e32 v130, 0, v100
	v_max_f32_e32 v131, 0, v101
	s_nop 1
	v_pk_add_f32 v[100:101], v[90:91], v[150:151]
	v_pk_add_f32 v[110:111], v[88:89], v[148:149]
	v_mfma_f32_16x16x32_f16 v[88:91], v[172:175], v[42:45], v[122:125]
	v_max_f32_e32 v112, 0, v100
	v_max_f32_e32 v113, 0, v101
	v_max_f32_e32 v110, 0, v110
	v_mfma_f32_16x16x32_f16 v[100:103], v[102:105], v[18:21], v[136:139]
	v_max_f32_e32 v111, 0, v111
	ds_write_b128 v71, v[130:133] offset:272
	ds_write_b128 v71, v[110:113] offset:4624
	v_mfma_f32_16x16x32_f16 v[88:91], v[188:191], v[50:53], v[88:91]
	v_mfma_f32_16x16x32_f16 v[100:103], v[172:175], v[22:25], v[100:103]
	v_mfma_f32_16x16x32_f16 v[96:99], v[176:179], v[58:61], v[96:99]
	s_nop 5
	v_add_f32_e64 v90, v90, v150
	v_add_f32_e64 v91, v91, v151
	v_pk_add_f32 v[88:89], v[88:89], v[148:149]
	v_max_f32_e32 v90, 0, v90
	v_max_f32_e32 v88, 0, v88
	v_max_f32_e32 v89, 0, v89
	v_max_f32_e32 v91, 0, v91
	ds_write_b128 v71, v[88:91] offset:8976
	v_mfma_f32_16x16x32_f16 v[88:91], v[188:191], v[30:33], v[100:103]
	v_mfma_f32_16x16x32_f16 v[100:103], v[176:179], v[42:45], v[126:129]
	v_mfma_f32_16x16x32_f16 v[96:99], v[192:195], v[184:187], v[96:99]
	s_nop 5
	v_add_f32_e64 v90, v90, v150
	v_add_f32_e64 v91, v91, v151
	v_pk_add_f32 v[88:89], v[88:89], v[148:149]
	v_max_f32_e32 v90, 0, v90
	v_max_f32_e32 v88, 0, v88
	v_max_f32_e32 v89, 0, v89
	v_max_f32_e32 v91, 0, v91
	ds_write_b128 v71, v[88:91] offset:13328
	v_mfma_f32_16x16x32_f16 v[88:91], v[176:179], v[46:49], v[168:171]
	v_add_f32_e64 v98, v98, v154
	v_add_f32_e64 v99, v99, v155
	v_pk_add_f32 v[96:97], v[96:97], v[152:153]
	v_max_f32_e32 v98, 0, v98
	v_mfma_f32_16x16x32_f16 v[88:91], v[192:195], v[62:65], v[88:91]
	v_max_f32_e32 v96, 0, v96
	v_max_f32_e32 v97, 0, v97
	v_max_f32_e32 v99, 0, v99
	ds_write_b128 v71, v[96:99] offset:336
	v_mfma_f32_16x16x32_f16 v[96:99], v[156:159], v[18:21], v[140:143]
	s_nop 2
	v_add_f32_e64 v90, v90, v154
	v_add_f32_e64 v91, v91, v155
	v_pk_add_f32 v[88:89], v[88:89], v[152:153]
	v_max_f32_e32 v90, 0, v90
	v_max_f32_e32 v88, 0, v88
	v_max_f32_e32 v89, 0, v89
	v_max_f32_e32 v91, 0, v91
	ds_write_b128 v71, v[88:91] offset:4688
	v_mfma_f32_16x16x32_f16 v[88:91], v[192:195], v[50:53], v[100:103]
	v_mfma_f32_16x16x32_f16 v[96:99], v[176:179], v[22:25], v[96:99]
	v_mfma_f32_16x16x32_f16 v[96:99], v[192:195], v[30:33], v[96:99]
	s_nop 5
	v_add_f32_e64 v90, v90, v154
	v_add_f32_e64 v91, v91, v155
	v_pk_add_f32 v[88:89], v[88:89], v[152:153]
	v_max_f32_e32 v90, 0, v90
	v_max_f32_e32 v88, 0, v88
	v_max_f32_e32 v89, 0, v89
	v_max_f32_e32 v91, 0, v91
	ds_write_b128 v71, v[88:91] offset:9040
	v_mfma_f32_16x16x32_f16 v[88:91], v[180:183], v[58:61], v[106:109]
	v_add_f32_e64 v98, v98, v154
	v_add_f32_e64 v99, v99, v155
	v_pk_add_f32 v[96:97], v[96:97], v[152:153]
	v_max_f32_e32 v98, 0, v98
	v_mfma_f32_16x16x32_f16 v[88:91], v[196:199], v[184:187], v[88:91]
	v_max_f32_e32 v96, 0, v96
	v_max_f32_e32 v97, 0, v97
	v_max_f32_e32 v99, 0, v99
	v_mfma_f32_16x16x32_f16 v[100:103], v[180:183], v[46:49], v[114:117]
	ds_write_b128 v71, v[96:99] offset:13392
	s_nop 2
	v_pk_add_f32 v[90:91], v[90:91], v[36:37]
	v_pk_add_f32 v[88:89], v[88:89], v[34:35]
	v_max_f32_e32 v90, 0, v90
	v_max_f32_e32 v88, 0, v88
	v_max_f32_e32 v89, 0, v89
	v_max_f32_e32 v91, 0, v91
	ds_write_b128 v71, v[88:91] offset:400
	v_mfma_f32_16x16x32_f16 v[88:91], v[196:199], v[62:65], v[100:103]
	v_mfma_f32_16x16x32_f16 v[96:99], v[164:167], v[18:21], v[144:147]
	v_mfma_f32_16x16x32_f16 v[100:103], v[180:183], v[42:45], v[160:163]
	s_nop 5
	v_add_f32_e64 v90, v90, v36
	v_add_f32_e64 v91, v91, v37
	v_pk_add_f32 v[88:89], v[88:89], v[34:35]
	v_max_f32_e32 v90, 0, v90
	v_max_f32_e32 v88, 0, v88
	v_max_f32_e32 v89, 0, v89
	v_max_f32_e32 v91, 0, v91
	ds_write_b128 v71, v[88:91] offset:4752
	v_mfma_f32_16x16x32_f16 v[88:91], v[180:183], v[22:25], v[96:99]
	v_mfma_f32_16x16x32_f16 v[100:103], v[196:199], v[50:53], v[100:103]
	v_mfma_f32_16x16x32_f16 v[88:91], v[196:199], v[30:33], v[88:91]
	v_mfma_f32_16x16x32_f16 v[10:13], v[14:17], v[66:69], v[10:13]
	s_nop 5
	v_add_f32_e64 v102, v102, v36
	v_add_f32_e64 v103, v103, v37
	v_pk_add_f32 v[100:101], v[100:101], v[34:35]
	v_pk_add_f32 v[36:37], v[90:91], v[36:37]
	v_mfma_f32_16x16x32_f16 v[6:9], v[14:17], v[18:21], v[6:9]
	v_add_f32_e64 v34, v88, v34
	v_add_f32_e64 v35, v89, v35
	v_max_f32_e32 v36, 0, v36
	v_max_f32_e32 v34, 0, v34
	v_mfma_f32_16x16x32_f16 v[54:57], v[26:29], v[58:61], v[54:57]
	v_max_f32_e32 v35, 0, v35
	v_max_f32_e32 v37, 0, v37
	ds_write_b128 v71, v[34:37] offset:13456
	v_mfma_f32_16x16x32_f16 v[46:49], v[26:29], v[46:49], v[118:121]
	v_max_f32_e32 v96, 0, v100
	v_max_f32_e32 v97, 0, v101
	v_max_f32_e32 v98, 0, v102
	v_mfma_f32_16x16x32_f16 v[10:13], v[26:29], v[42:45], v[10:13]
	v_max_f32_e32 v99, 0, v103
	ds_write_b128 v71, v[96:99] offset:9104
	v_mfma_f32_16x16x32_f16 v[6:9], v[26:29], v[22:25], v[6:9]
	v_mfma_f32_16x16x32_f16 v[34:37], v[38:41], v[184:187], v[54:57]
	v_mfma_f32_16x16x32_f16 v[46:49], v[38:41], v[62:65], v[46:49]
	v_mfma_f32_16x16x32_f16 v[10:13], v[38:41], v[50:53], v[10:13]
	s_nop 5
	v_add_f32_e64 v36, v36, v4
	v_add_f32_e64 v37, v37, v5
	v_pk_add_f32 v[34:35], v[34:35], v[2:3]
	v_max_f32_e32 v36, 0, v36
	v_mfma_f32_16x16x32_f16 v[6:9], v[38:41], v[30:33], v[6:9]
	v_max_f32_e32 v34, 0, v34
	v_max_f32_e32 v35, 0, v35
	v_max_f32_e32 v37, 0, v37
	ds_write_b128 v71, v[34:37] offset:464
	v_pk_add_f32 v[36:37], v[48:49], v[4:5]
	v_pk_add_f32 v[34:35], v[46:47], v[2:3]
	v_pk_add_f32 v[12:13], v[12:13], v[4:5]
	v_pk_add_f32 v[10:11], v[10:11], v[2:3]
	v_pk_add_f32 v[4:5], v[8:9], v[4:5]
	v_pk_add_f32 v[2:3], v[6:7], v[2:3]
	v_max_f32_e32 v34, 0, v34
	v_max_f32_e32 v35, 0, v35
	v_max_f32_e32 v36, 0, v36
	v_max_f32_e32 v37, 0, v37
	v_max_f32_e32 v10, 0, v10
	v_max_f32_e32 v11, 0, v11
	v_max_f32_e32 v12, 0, v12
	v_max_f32_e32 v13, 0, v13
	v_max_f32_e32 v2, 0, v2
	v_max_f32_e32 v3, 0, v3
	v_max_f32_e32 v4, 0, v4
	v_max_f32_e32 v5, 0, v5
	ds_write_b128 v71, v[34:37] offset:4816
	ds_write_b128 v71, v[10:13] offset:9168
	ds_write_b128 v71, v[2:5] offset:13520
	s_and_saveexec_b64 s[2:3], vcc
	s_cbranch_execz .LBB2_8
	v_mov_b32_e32 v2, 0
	v_add_u32_e32 v0, 0, v70
	v_mov_b32_e32 v3, v2
	v_mov_b32_e32 v4, v2
	v_mov_b32_e32 v5, v2
	ds_write_b128 v0, v[2:5]

_ZN12_GLOBAL__N_14k_fcEPKtPKiS1_PKfS5_Pf:
	s_load_dwordx8 s[4:11], s[0:1], 0x0
	s_load_dwordx4 s[12:15], s[0:1], 0x20
	s_and_b32 s3, s2, 7
	s_lshr_b32 s20, s2, 3
	s_lshr_b32 s19, s20, 2
	s_lshl_b32 s3, s3, 3
	s_add_u32 s19, s19, s3
	s_and_b32 s20, s20, 3
	v_lshrrev_b32_e32 v1, 6, v0
	v_and_b32_e32 v12, 63, v0
	v_and_b32_e32 v13, 15, v0
	v_readfirstlane_b32 s16, v1
	v_lshrrev_b32_e32 v14, 4, v12
	s_nop 3
	s_lshr_b32 s17, s16, 2
	s_and_b32 s18, s16, 3
	v_lshrrev_b32_e32 v70, 2, v12
	s_lshl_b32 s90, s19, 8
	s_lshl_b32 s91, s16, 5
	s_add_u32 s90, s90, s91
	v_add_u32_e32 v73, s90, v70
	v_add_u32_e32 v74, 16, v73
	v_lshlrev_b32_e32 v75, 3, v73
	v_lshlrev_b32_e32 v76, 3, v74
	s_waitcnt lgkmcnt(0)
	global_load_dwordx2 v[64:65], v75, s[6:7]
	global_load_dwordx2 v[66:67], v76, s[6:7]
	s_mul_i32 s90, s20, 0x180
	s_mul_i32 s91, s18, 96
	s_add_u32 s90, s90, s91
	v_lshl_add_u32 v15, v14, 2, s90
	v_lshlrev_b32_e32 v15, 2, v15
	global_load_dwordx4 v[16:19], v15, s[10:11] offset:0
	global_load_dwordx4 v[20:23], v15, s[10:11] offset:64
	global_load_dwordx4 v[24:27], v15, s[10:11] offset:128
	global_load_dwordx4 v[28:31], v15, s[10:11] offset:192
	global_load_dwordx4 v[32:35], v15, s[10:11] offset:256
	global_load_dwordx4 v[36:39], v15, s[10:11] offset:320
	v_mul_u32_u24_e32 v77, 0x1800, v13
	v_add_u32_e32 v77, v77, v15
	v_mov_b32_e32 v40, 0
	v_mov_b32_e32 v41, 0
	v_mov_b32_e32 v42, 0
	v_mov_b32_e32 v43, 0
	v_mov_b32_e32 v44, 0
	v_mov_b32_e32 v45, 0
	v_mov_b32_e32 v46, 0
	v_mov_b32_e32 v47, 0
	v_mov_b32_e32 v48, 0
	v_mov_b32_e32 v49, 0
	v_mov_b32_e32 v50, 0
	v_mov_b32_e32 v51, 0
	v_mov_b32_e32 v52, 0
	v_mov_b32_e32 v53, 0
	v_mov_b32_e32 v54, 0
	v_mov_b32_e32 v55, 0
	v_mov_b32_e32 v56, 0
	v_mov_b32_e32 v57, 0
	v_mov_b32_e32 v58, 0
	v_mov_b32_e32 v59, 0
	v_mov_b32_e32 v60, 0
	v_mov_b32_e32 v61, 0
	v_mov_b32_e32 v62, 0
	v_mov_b32_e32 v63, 0
	s_mov_b32 exec_lo, 0xff00ff
	s_mov_b32 exec_hi, 0xff00ff
	global_load_dwordx4 v[40:43], v77, s[12:13] offset:0
	global_load_dwordx4 v[44:47], v77, s[12:13] offset:64
	global_load_dwordx4 v[48:51], v77, s[12:13] offset:128
	global_load_dwordx4 v[52:55], v77, s[12:13] offset:192
	global_load_dwordx4 v[56:59], v77, s[12:13] offset:256
	global_load_dwordx4 v[60:63], v77, s[12:13] offset:320
	s_mov_b64 exec, -1
	v_lshlrev_b32_e32 v15, 6, v13
	v_lshl_add_u32 v15, v14, 4, v15
	v_lshrrev_b32_e32 v78, 3, v13
	v_lshlrev_b32_e32 v78, 5, v78
	v_xor_b32_e32 v15, v15, v78
	s_lshl_b32 s90, s17, 13
	v_add_u32_e32 v1, s90, v15
	v_add_u32_e32 v2, 0x14000, v1
	s_mul_i32 s90, s18, 0x1800
	s_add_u32 s90, s90, 0x4000
	v_add_u32_e32 v3, s90, v15
	v_add_u32_e32 v4, 0x14000, v3
	v_and_b32_e32 v71, 3, v12
	v_lshrrev_b32_e32 v72, 5, v12
	v_lshlrev_b32_e32 v72, 1, v72
	v_xor_b32_e32 v71, v71, v72
	v_lshlrev_b32_e32 v71, 4, v71
	v_lshl_add_u32 v11, v70, 6, v71
	s_mul_i32 s90, s20, 0x180
	s_mul_i32 s91, s16, 48
	s_add_u32 s90, s90, s91
	s_lshl_b32 s90, s90, 6
	s_add_u32 s28, s8, s90
	s_addc_u32 s29, s9, 0
	s_add_u32 s30, s28, 0x18000
	s_addc_u32 s31, s29, 0
	s_add_u32 s32, s28, 0x400
	s_addc_u32 s33, s29, 0
	s_add_u32 s34, s32, 0x18000
	s_addc_u32 s35, s33, 0
	s_add_u32 s36, s28, 0x800
	s_addc_u32 s37, s29, 0
	s_add_u32 s38, s36, 0x18000
	s_addc_u32 s39, s37, 0
	s_mov_b64 s[24:25], s[4:5]
	s_add_u32 s26, s4, 0x40
	s_addc_u32 s27, s5, 0
	s_add_u32 s96, s4, 0x1000000
	s_addc_u32 s97, s5, 0
	s_lshl_b32 s22, s16, 11
	s_mul_i32 s23, s16, 0xc00
	s_add_u32 s23, s23, 0x4000
	s_mov_b32 s21, 0
	s_lshr_b32 s92, s19, 1
	s_lshl_b32 s92, s92, 9
	s_movk_i32 s93, 0x1ff
	s_movk_i32 s94, 0x200
	s_waitcnt vmcnt(12)
	v_med3_i32 v64, v64, 0, s93
	v_med3_i32 v65, v65, 1, s94
	v_med3_i32 v66, v66, 0, s93
	v_med3_i32 v67, v67, 1, s94
	v_add_u32_e32 v64, s92, v64
	v_add_u32_e32 v66, s92, v66
	v_add_u32_e32 v65, s92, v65
	v_add_u32_e32 v67, s92, v67
	v_add_u32_e32 v65, -1, v65
	v_add_u32_e32 v67, -1, v67
	v_lshl_add_u32 v5, v64, 10, v71
	v_lshl_add_u32 v6, v66, 10, v71
	v_lshl_add_u32 v7, v73, 10, v71
	v_lshl_add_u32 v8, v74, 10, v71
	v_lshl_add_u32 v9, v65, 10, v71
	v_lshl_add_u32 v10, v67, 10, v71
	s_cmp_lg_u32 s17, 0
	s_cbranch_scc1 .Lfc_h1_entry
	s_add_u32 m0, s22, 0x0
	s_nop 0
	global_load_lds_dwordx4 v5, s[24:25]
	s_add_u32 m0, s22, 0x400
	s_nop 0
	global_load_lds_dwordx4 v6, s[24:25]
	s_add_u32 m0, s23, 0x0
	s_nop 0
	global_load_lds_dwordx4 v11, s[28:29]
	s_add_u32 m0, s23, 0x400
	s_nop 0
	global_load_lds_dwordx4 v11, s[32:33]
	s_add_u32 m0, s23, 0x800
	s_nop 0
	global_load_lds_dwordx4 v11, s[36:37]
	s_add_u32 s24, s24, 0x80
	s_addc_u32 s25, s25, 0
	s_add_u32 s28, s28, 0x30000
	s_addc_u32 s29, s29, 0
	s_add_u32 s32, s32, 0x30000
	s_addc_u32 s33, s33, 0
	s_add_u32 s36, s36, 0x30000
	s_addc_u32 s37, s37, 0
	s_add_u32 m0, s22, 0xa000
	s_nop 0
	global_load_lds_dwordx4 v5, s[26:27]
	s_add_u32 m0, s22, 0xa400
	s_nop 0
	global_load_lds_dwordx4 v6, s[26:27]
	s_add_u32 m0, s23, 0xa000
	s_nop 0
	global_load_lds_dwordx4 v11, s[30:31]
	s_add_u32 m0, s23, 0xa400
	s_nop 0
	global_load_lds_dwordx4 v11, s[34:35]
	s_add_u32 m0, s23, 0xa800
	s_nop 0
	global_load_lds_dwordx4 v11, s[38:39]
	s_add_u32 s26, s26, 0x80
	s_addc_u32 s27, s27, 0
	s_add_u32 s30, s30, 0x30000
	s_addc_u32 s31, s31, 0
	s_add_u32 s34, s34, 0x30000
	s_addc_u32 s35, s35, 0
	s_add_u32 s38, s38, 0x30000
	s_addc_u32 s39, s39, 0
	s_add_u32 m0, s22, 0x14000
	s_nop 0
	global_load_lds_dwordx4 v5, s[24:25]
	s_add_u32 m0, s22, 0x14400
	s_nop 0
	global_load_lds_dwordx4 v6, s[24:25]
	s_add_u32 m0, s23, 0x14000
	s_nop 0
	global_load_lds_dwordx4 v11, s[28:29]
	s_add_u32 m0, s23, 0x14400
	s_nop 0
	global_load_lds_dwordx4 v11, s[32:33]
	s_add_u32 m0, s23, 0x14800
	s_nop 0
	global_load_lds_dwordx4 v11, s[36:37]
	s_add_u32 s24, s24, 0x80
	s_addc_u32 s25, s25, 0
	s_add_u32 s28, s28, 0x30000
	s_addc_u32 s29, s29, 0
	s_add_u32 s32, s32, 0x30000
	s_addc_u32 s33, s33, 0
	s_add_u32 s36, s36, 0x30000
	s_addc_u32 s37, s37, 0
	s_add_u32 m0, s22, 0x1e000
	s_nop 0
	global_load_lds_dwordx4 v5, s[26:27]
	s_add_u32 m0, s22, 0x1e400
	s_nop 0
	global_load_lds_dwordx4 v6, s[26:27]
	s_add_u32 m0, s23, 0x1e000
	s_nop 0
	global_load_lds_dwordx4 v11, s[30:31]
	s_add_u32 m0, s23, 0x1e400
	s_nop 0
	global_load_lds_dwordx4 v11, s[34:35]
	s_add_u32 m0, s23, 0x1e800
	s_nop 0
	global_load_lds_dwordx4 v11, s[38:39]
	s_add_u32 s26, s26, 0x80
	s_addc_u32 s27, s27, 0
	s_add_u32 s30, s30, 0x30000
	s_addc_u32 s31, s31, 0
	s_add_u32 s34, s34, 0x30000
	s_addc_u32 s35, s35, 0
	s_add_u32 s38, s38, 0x30000
	s_addc_u32 s39, s39, 0
	s_waitcnt vmcnt(20)
	v_cvt_pk_f16_f32 v12, v40, v41
	v_cvt_pk_f16_f32 v13, v42, v43
	v_cvt_pk_f16_f32 v14, v44, v45
	v_cvt_pk_f16_f32 v15, v46, v47
	v_cvt_pk_f16_f32 v56, v56, v57
	v_cvt_pk_f16_f32 v57, v58, v59
	v_cvt_pk_f16_f32 v58, v60, v61
	v_cvt_pk_f16_f32 v59, v62, v63
	v_cvt_pk_f16_f32 v60, v48, v49
	v_cvt_pk_f16_f32 v61, v50, v51
	v_cvt_pk_f16_f32 v62, v52, v53
	v_cvt_pk_f16_f32 v63, v54, v55
	v_mov_b32_e32 v64, v16
	v_mov_b32_e32 v65, v17
	v_mov_b32_e32 v66, v18
	v_mov_b32_e32 v67, v19
	v_mov_b32_e32 v68, v20
	v_mov_b32_e32 v69, v21
	v_mov_b32_e32 v70, v22
	v_mov_b32_e32 v71, v23
	v_mov_b32_e32 v72, v24
	v_mov_b32_e32 v73, v25
	v_mov_b32_e32 v74, v26
	v_mov_b32_e32 v75, v27
	v_mov_b32_e32 v76, v28
	v_mov_b32_e32 v77, v29
	v_mov_b32_e32 v78, v30
	v_mov_b32_e32 v79, v31
	v_mov_b32_e32 v80, v32
	v_mov_b32_e32 v81, v33
	v_mov_b32_e32 v82, v34
	v_mov_b32_e32 v83, v35
	v_mov_b32_e32 v84, v36
	v_mov_b32_e32 v85, v37
	v_mov_b32_e32 v86, v38
	v_mov_b32_e32 v87, v39
	v_mov_b32_e32 v88, v16
	v_mov_b32_e32 v89, v17
	v_mov_b32_e32 v90, v18
	v_mov_b32_e32 v91, v19
	v_mov_b32_e32 v92, v20
	v_mov_b32_e32 v93, v21
	v_mov_b32_e32 v94, v22
	v_mov_b32_e32 v95, v23
	v_mov_b32_e32 v96, v24
	v_mov_b32_e32 v97, v25
	v_mov_b32_e32 v98, v26
	v_mov_b32_e32 v99, v27
	v_mov_b32_e32 v100, v28
	v_mov_b32_e32 v101, v29
	v_mov_b32_e32 v102, v30
	v_mov_b32_e32 v103, v31
	v_mov_b32_e32 v104, v32
	v_mov_b32_e32 v105, v33
	v_mov_b32_e32 v106, v34
	v_mov_b32_e32 v107, v35
	v_mov_b32_e32 v108, v36
	v_mov_b32_e32 v109, v37
	v_mov_b32_e32 v110, v38
	v_mov_b32_e32 v111, v39
	v_mov_b32_e32 v112, v16
	v_mov_b32_e32 v113, v17
	v_mov_b32_e32 v114, v18
	v_mov_b32_e32 v115, v19
	v_mov_b32_e32 v116, v20
	v_mov_b32_e32 v117, v21
	v_mov_b32_e32 v118, v22
	v_mov_b32_e32 v119, v23
	v_mov_b32_e32 v120, v24
	v_mov_b32_e32 v121, v25
	v_mov_b32_e32 v122, v26
	v_mov_b32_e32 v123, v27
	v_mov_b32_e32 v124, v28
	v_mov_b32_e32 v125, v29
	v_mov_b32_e32 v126, v30
	v_mov_b32_e32 v127, v31
	v_mov_b32_e32 v128, v32
	v_mov_b32_e32 v129, v33
	v_mov_b32_e32 v130, v34
	v_mov_b32_e32 v131, v35
	v_mov_b32_e32 v132, v36
	v_mov_b32_e32 v133, v37
	v_mov_b32_e32 v134, v38
	v_mov_b32_e32 v135, v39
	v_mov_b32_e32 v136, v16
	v_mov_b32_e32 v137, v17
	v_mov_b32_e32 v138, v18
	v_mov_b32_e32 v139, v19
	v_mov_b32_e32 v140, v20
	v_mov_b32_e32 v141, v21
	v_mov_b32_e32 v142, v22
	v_mov_b32_e32 v143, v23
	v_mov_b32_e32 v144, v24
	v_mov_b32_e32 v145, v25
	v_mov_b32_e32 v146, v26
	v_mov_b32_e32 v147, v27
	v_mov_b32_e32 v148, v28
	v_mov_b32_e32 v149, v29
	v_mov_b32_e32 v150, v30
	v_mov_b32_e32 v151, v31
	v_mov_b32_e32 v152, v32
	v_mov_b32_e32 v153, v33
	v_mov_b32_e32 v154, v34
	v_mov_b32_e32 v155, v35
	v_mov_b32_e32 v156, v36
	v_mov_b32_e32 v157, v37
	v_mov_b32_e32 v158, v38
	v_mov_b32_e32 v159, v39
	v_mov_b32_e32 v160, v16
	v_mov_b32_e32 v161, v17
	v_mov_b32_e32 v162, v18
	v_mov_b32_e32 v163, v19
	v_mov_b32_e32 v164, v20
	v_mov_b32_e32 v165, v21
	v_mov_b32_e32 v166, v22
	v_mov_b32_e32 v167, v23
	v_mov_b32_e32 v168, v24
	v_mov_b32_e32 v169, v25
	v_mov_b32_e32 v170, v26
	v_mov_b32_e32 v171, v27
	v_mov_b32_e32 v172, v28
	v_mov_b32_e32 v173, v29
	v_mov_b32_e32 v174, v30
	v_mov_b32_e32 v175, v31
	v_mov_b32_e32 v176, v32
	v_mov_b32_e32 v177, v33
	v_mov_b32_e32 v178, v34
	v_mov_b32_e32 v179, v35
	v_mov_b32_e32 v180, v36
	v_mov_b32_e32 v181, v37
	v_mov_b32_e32 v182, v38
	v_mov_b32_e32 v183, v39
	v_mov_b32_e32 v184, v16
	v_mov_b32_e32 v185, v17
	v_mov_b32_e32 v186, v18
	v_mov_b32_e32 v187, v19
	v_mov_b32_e32 v188, v20
	v_mov_b32_e32 v189, v21
	v_mov_b32_e32 v190, v22
	v_mov_b32_e32 v191, v23
	v_mov_b32_e32 v192, v24
	v_mov_b32_e32 v193, v25
	v_mov_b32_e32 v194, v26
	v_mov_b32_e32 v195, v27
	v_mov_b32_e32 v196, v28
	v_mov_b32_e32 v197, v29
	v_mov_b32_e32 v198, v30
	v_mov_b32_e32 v199, v31
	v_mov_b32_e32 v200, v32
	v_mov_b32_e32 v201, v33
	v_mov_b32_e32 v202, v34
	v_mov_b32_e32 v203, v35
	v_mov_b32_e32 v204, v36
	v_mov_b32_e32 v205, v37
	v_mov_b32_e32 v206, v38
	v_mov_b32_e32 v207, v39
	v_mov_b32_e32 v208, v16
	v_mov_b32_e32 v209, v17
	v_mov_b32_e32 v210, v18
	v_mov_b32_e32 v211, v19
	v_mov_b32_e32 v212, v20
	v_mov_b32_e32 v213, v21
	v_mov_b32_e32 v214, v22
	v_mov_b32_e32 v215, v23
	v_mov_b32_e32 v216, v24
	v_mov_b32_e32 v217, v25
	v_mov_b32_e32 v218, v26
	v_mov_b32_e32 v219, v27
	v_mov_b32_e32 v220, v28
	v_mov_b32_e32 v221, v29
	v_mov_b32_e32 v222, v30
	v_mov_b32_e32 v223, v31
	v_mov_b32_e32 v224, v32
	v_mov_b32_e32 v225, v33
	v_mov_b32_e32 v226, v34
	v_mov_b32_e32 v227, v35
	v_mov_b32_e32 v228, v36
	v_mov_b32_e32 v229, v37
	v_mov_b32_e32 v230, v38
	v_mov_b32_e32 v231, v39
	v_mov_b32_e32 v232, v16
	v_mov_b32_e32 v233, v17
	v_mov_b32_e32 v234, v18
	v_mov_b32_e32 v235, v19
	v_mov_b32_e32 v236, v20
	v_mov_b32_e32 v237, v21
	v_mov_b32_e32 v238, v22
	v_mov_b32_e32 v239, v23
	v_mov_b32_e32 v240, v24
	v_mov_b32_e32 v241, v25
	v_mov_b32_e32 v242, v26
	v_mov_b32_e32 v243, v27
	v_mov_b32_e32 v244, v28
	v_mov_b32_e32 v245, v29
	v_mov_b32_e32 v246, v30
	v_mov_b32_e32 v247, v31
	v_mov_b32_e32 v248, v32
	v_mov_b32_e32 v249, v33
	v_mov_b32_e32 v250, v34
	v_mov_b32_e32 v251, v35
	v_mov_b32_e32 v252, v36
	v_mov_b32_e32 v253, v37
	v_mov_b32_e32 v254, v38
	v_mov_b32_e32 v255, v39
	s_waitcnt vmcnt(15)
	s_barrier

.Lfc_sw_4:
	s_mov_b64 s[24:25], s[96:97]
	s_add_u32 s26, s96, 0x40
	s_addc_u32 s27, s97, 0
	s_mov_b64 s[96:97], s[4:5]
	v_mov_b32_e32 v5, v7
	v_mov_b32_e32 v6, v8
	v_mov_b32_e32 v7, v9
	v_mov_b32_e32 v8, v10

.Lfc_tail:
	s_waitcnt lgkmcnt(0)
	s_barrier
	v_lshrrev_b32_e32 v2, 1, v0
	v_and_b32_e32 v3, 1, v0
	v_lshlrev_b32_e32 v4, 5, v2
	v_lshl_add_u32 v4, v3, 4, v4
	ds_read_b128 v[16:19], v4
	ds_read_b128 v[20:23], v4 offset:8192
	ds_read_b128 v[24:27], v4 offset:16384
	ds_read_b128 v[28:31], v4 offset:24576
	s_lshl_b32 s90, s20, 20
	s_lshl_b32 s91, s19, 13
	s_add_u32 s90, s90, s91
	s_add_u32 s14, s14, s90
	s_addc_u32 s15, s15, 0
	s_add_u32 s92, s14, 0x80000
	s_addc_u32 s93, s15, 0
	s_waitcnt lgkmcnt(0)
	v_pk_add_f32 v[16:17], v[16:17], v[20:21]
	v_pk_add_f32 v[18:19], v[18:19], v[22:23]
	v_pk_add_f32 v[24:25], v[24:25], v[28:29]
	v_pk_add_f32 v[26:27], v[26:27], v[30:31]
	global_store_dwordx4 v4, v[16:19], s[14:15]
	global_store_dwordx4 v4, v[24:27], s[92:93]
	s_endpgm
	.p2align	8
